# baseline (speedup 1.0000x reference)
_Z9feat_gemmPKDF16_S0_PDF16_:
	s_load_dwordx4 s[4:7], s[0:1], 0x8
	s_load_dwordx2 s[8:9], s[0:1], 0x0
	s_lshr_b32 s10, s2, 6
	s_lshl_b32 s10, s10, 3
	s_and_b32 s11, s2, 7
	s_or_b32 s10, s10, s11
	s_bfe_u32 s11, s2, 0x30003
	s_mul_i32 s12, s10, 0x44
	s_lshr_b32 s14, s12, 4
	s_lshl_b32 s15, s14, 3
	s_sub_u32 s15, 0x441, s15
	v_cvt_f32_u32_e32 v174, s15
	v_sqrt_f32_e32 v174, v174
	v_and_b32_e32 v170, 63, v0
	v_lshrrev_b32_e32 v171, 6, v0
	v_sub_f32_e32 v174, 0x42040000, v174
	v_fmaak_f32 v174, 0.5, v174, 0x3c23d70a
	v_cvt_u32_f32_e32 v174, v174
	v_lshlrev_b32_e32 v160, 4, v170
	v_readfirstlane_b32 s13, v174
	s_sub_u32 s15, 33, s13
	s_mul_i32 s15, s15, s13
	s_lshr_b32 s15, s15, 1
	s_sub_u32 s14, s14, s15
	s_add_u32 s14, s14, s13
	s_bfe_u32 s46, s12, 0x20002
	v_and_b32_e32 v172, 31, v170
	v_readfirstlane_b32 s33, v171
	v_lshrrev_b32_e32 v173, 5, v170
	s_lshl_b32 s35, s33, 11
	s_lshl_b32 s34, s11, 8
	s_lshl_b32 s36, s33, 5
	s_add_u32 s34, s34, s36
	v_add_lshl_u32 v165, v172, s34, 4
	v_add_u32_e32 v166, 0x8000, v165
	v_lshl_add_u32 v164, v173, 15, v165
	v_add_u32_e32 v168, s35, v160
	v_mov_b32_e32 v161, v160
	s_waitcnt lgkmcnt(0)
	s_lshl_b32 s36, s12, 12
	s_add_u32 s20, s4, s36
	s_addc_u32 s21, s5, 0
	s_min_u32 s43, s13, 15
	s_min_u32 s44, s14, 15
	s_lshl_b32 s45, s44, 16
	s_add_u32 s24, s8, s45
	s_addc_u32 s25, s9, 0
	s_add_u32 s26, s24, 0x100000
	s_addc_u32 s27, s25, 0
	s_lshl_b32 s45, s43, 16
	s_add_u32 s28, s8, s45
	s_addc_u32 s29, s9, 0
	s_add_u32 s30, s28, 0x100000
	s_addc_u32 s31, s29, 0
	global_load_dwordx4 v[36:39], v164, s[24:25] nt
	global_load_dwordx4 v[32:35], v164, s[26:27] nt
	global_load_dwordx4 v[40:43], v165, s[28:29] nt
	global_load_dwordx4 v[44:47], v166, s[28:29] nt
	global_load_dwordx4 v[48:51], v165, s[30:31] nt
	global_load_dwordx4 v[52:55], v166, s[30:31] nt
	s_mov_b32 s17, 0
	s_mov_b32 s18, 0
	s_mov_b32 s19, 0
	s_mov_b32 s22, 0
	s_sub_u32 s39, 5, s46
	s_mov_b32 s38, 0
